# lean GEMM epilogue also at E1-odd and C6 (C6: relu-square, last rs dword loaded late)
# speedup vs baseline: 1.0158x; 1.0096x over previous
.LBB0_416:
	s_ashr_i32 s23, s22, 31
	s_lshl_b64 s[8:9], s[22:23], 19
	s_add_u32 s24, s34, s8
	s_addc_u32 s25, s35, s9
	s_and_b64 s[8:9], s[40:41], exec
	s_cselect_b32 s5, s25, s29
	s_cselect_b32 s8, s24, s28
	s_ashr_i32 s21, s20, 31
	s_lshl_b64 s[26:27], s[20:21], 19
	s_add_u32 s26, s36, s26
	s_addc_u32 s27, s37, s27
	s_and_b64 s[30:31], s[40:41], exec
	s_cselect_b32 s9, s27, s7
	s_cselect_b32 s21, s26, s6
	s_add_u32 s23, s6, 0x100
	s_addc_u32 s33, s7, 0
	s_add_u32 s6, s28, 0x40080
	v_mov_b32_e32 v2, 0
	s_addc_u32 s7, s29, 0
	s_mov_b32 s42, -2
	s_cmp_lg_u32 s53, 1
	s_cbranch_scc1 .Lskipz_e1o
	v_mov_b32_e32 v3, v2
	v_mov_b32_e32 v4, v2
	v_mov_b32_e32 v5, v2
	v_mov_b32_e32 v6, v2
	v_mov_b32_e32 v7, v2
	v_mov_b32_e32 v8, v2
	v_mov_b32_e32 v9, v2
	v_mov_b32_e32 v14, v2
	v_mov_b32_e32 v15, v2
	v_mov_b32_e32 v16, v2
	v_mov_b32_e32 v17, v2
	v_mov_b32_e32 v22, v2
	v_mov_b32_e32 v23, v2
	v_mov_b32_e32 v24, v2
	v_mov_b32_e32 v25, v2
	v_mov_b32_e32 v30, v2
	v_mov_b32_e32 v31, v2
	v_mov_b32_e32 v32, v2
	v_mov_b32_e32 v33, v2
	v_mov_b32_e32 v38, v2
	v_mov_b32_e32 v39, v2
	v_mov_b32_e32 v40, v2
	v_mov_b32_e32 v41, v2
	v_mov_b32_e32 v46, v2
	v_mov_b32_e32 v47, v2
	v_mov_b32_e32 v48, v2
	v_mov_b32_e32 v49, v2
	v_mov_b32_e32 v54, v2
	v_mov_b32_e32 v55, v2
	v_mov_b32_e32 v56, v2
	v_mov_b32_e32 v57, v2
	v_mov_b32_e32 v10, v2
	v_mov_b32_e32 v11, v2
	v_mov_b32_e32 v12, v2
	v_mov_b32_e32 v13, v2
	v_mov_b32_e32 v18, v2
	v_mov_b32_e32 v19, v2
	v_mov_b32_e32 v20, v2
	v_mov_b32_e32 v21, v2
	v_mov_b32_e32 v26, v2
	v_mov_b32_e32 v27, v2
	v_mov_b32_e32 v28, v2
	v_mov_b32_e32 v29, v2
	v_mov_b32_e32 v34, v2
	v_mov_b32_e32 v35, v2
	v_mov_b32_e32 v36, v2
	v_mov_b32_e32 v37, v2
	v_mov_b32_e32 v42, v2
	v_mov_b32_e32 v43, v2
	v_mov_b32_e32 v44, v2
	v_mov_b32_e32 v45, v2
	v_mov_b32_e32 v50, v2
	v_mov_b32_e32 v51, v2
	v_mov_b32_e32 v52, v2
	v_mov_b32_e32 v53, v2
	v_mov_b32_e32 v58, v2
	v_mov_b32_e32 v59, v2
	v_mov_b32_e32 v60, v2
	v_mov_b32_e32 v61, v2
	v_mov_b32_e32 v62, v2
	v_mov_b32_e32 v63, v2
	v_mov_b32_e32 v64, v2
	v_mov_b32_e32 v65, v2
	v_mov_b32_e32 v66, v2
	v_mov_b32_e32 v67, v2
	v_mov_b32_e32 v68, v2
	v_mov_b32_e32 v69, v2
	v_mov_b32_e32 v70, v2
	v_mov_b32_e32 v71, v2
	v_mov_b32_e32 v72, v2
	v_mov_b32_e32 v73, v2
	v_mov_b32_e32 v78, v2
	v_mov_b32_e32 v79, v2
	v_mov_b32_e32 v80, v2
	v_mov_b32_e32 v81, v2
	v_mov_b32_e32 v86, v2
	v_mov_b32_e32 v87, v2
	v_mov_b32_e32 v88, v2
	v_mov_b32_e32 v89, v2
	v_mov_b32_e32 v94, v2
	v_mov_b32_e32 v95, v2
	v_mov_b32_e32 v96, v2
	v_mov_b32_e32 v97, v2
	v_mov_b32_e32 v102, v2
	v_mov_b32_e32 v103, v2
	v_mov_b32_e32 v104, v2
	v_mov_b32_e32 v105, v2
	v_mov_b32_e32 v110, v2
	v_mov_b32_e32 v111, v2
	v_mov_b32_e32 v112, v2
	v_mov_b32_e32 v113, v2
	v_mov_b32_e32 v118, v2
	v_mov_b32_e32 v119, v2
	v_mov_b32_e32 v120, v2
	v_mov_b32_e32 v121, v2
	v_mov_b32_e32 v74, v2
	v_mov_b32_e32 v75, v2
	v_mov_b32_e32 v76, v2
	v_mov_b32_e32 v77, v2
	v_mov_b32_e32 v82, v2
	v_mov_b32_e32 v83, v2
	v_mov_b32_e32 v84, v2
	v_mov_b32_e32 v85, v2
	v_mov_b32_e32 v90, v2
	v_mov_b32_e32 v91, v2
	v_mov_b32_e32 v92, v2
	v_mov_b32_e32 v93, v2
	v_mov_b32_e32 v98, v2
	v_mov_b32_e32 v99, v2
	v_mov_b32_e32 v100, v2
	v_mov_b32_e32 v101, v2
	v_mov_b32_e32 v106, v2
	v_mov_b32_e32 v107, v2
	v_mov_b32_e32 v108, v2
	v_mov_b32_e32 v109, v2
	v_mov_b32_e32 v114, v2
	v_mov_b32_e32 v115, v2
	v_mov_b32_e32 v116, v2
	v_mov_b32_e32 v117, v2
	v_mov_b32_e32 v122, v2
	v_mov_b32_e32 v123, v2
	v_mov_b32_e32 v124, v2
	v_mov_b32_e32 v125, v2
	v_mov_b32_e32 v126, v2
	v_mov_b32_e32 v127, v2
	v_mov_b32_e32 v128, v2
	v_mov_b32_e32 v129, v2
.Lskipz_e1o:
	v_and_b32_e32 v130, 8, v187
	v_and_b32_e32 v131, 16, v187
	v_lshlrev_b32_e32 v130, 2, v130
	v_lshl_add_u32 v130, v131, 3, v130
	v_lshl_add_u32 v131, s4, 8, v185
	v_add_u32_e32 v130, v130, v131
	v_mov_b32_e32 v131, 0
	v_lshl_add_u64 v[130:131], v[130:131], 4, s[16:17]
	global_load_dwordx4 v[240:243], v[130:131], off
	global_load_dwordx2 v[244:245], v[130:131], off offset:256
	global_load_dword v184, v[130:131], off offset:264
	global_load_dword v189, v[130:131], off offset:268
.LBB0_417:
	s_add_u32 s28, s6, 0xfffc0080
	s_addc_u32 s29, s7, -1
	s_add_i32 s43, 0, 0x10000
	s_cmp_eq_u32 s42, 12
	s_cselect_b32 s31, s5, s29
	s_cselect_b32 s30, s8, s28
	s_cselect_b32 s29, s9, s33
	s_cselect_b32 s28, s21, s23
	s_add_i32 s63, 0, 0x14000
	v_add_u32_e32 v142, s43, v186
	v_add_u32_e32 v168, s63, v186
	ds_read_b128 v[130:133], v142
	ds_read_b128 v[134:137], v142 offset:1024
	ds_read_b128 v[138:141], v142 offset:2048
	ds_read_b128 v[142:145], v142 offset:3072
	ds_read_b128 v[146:149], v168
	ds_read_b128 v[150:153], v168 offset:1024
	ds_read_b128 v[154:157], v168 offset:2048
	ds_read_b128 v[168:171], v168 offset:3072
	v_lshl_add_u64 v[216:217], s[6:7], 0, v[166:167]
	s_add_i32 m0, s45, 0xc000
	ds_read_b128 v[172:175], v188
	ds_read_b128 v[176:179], v188 offset:1024
	ds_read_b128 v[180:183], v188 offset:2048
	ds_read_b128 v[190:193], v188 offset:3072
	ds_read_b128 v[194:197], v188 offset:4096
	ds_read_b128 v[198:201], v188 offset:5120
	ds_read_b128 v[202:205], v188 offset:6144
	ds_read_b128 v[206:209], v188 offset:7168
	global_load_lds_dwordx4 v[216:217], off
	v_lshl_add_u64 v[216:217], s[6:7], 0, v[164:165]
	s_add_i32 m0, s45, 0xe000
	s_nop 0
	global_load_lds_dwordx4 v[216:217], off
	s_waitcnt vmcnt(8)
	s_waitcnt lgkmcnt(0)
	s_barrier
	s_setprio 1
	s_waitcnt lgkmcnt(0)
	v_mfma_f32_16x16x32_bf16 v[126:129], v[130:133], v[172:175], v[126:129]
	v_mfma_f32_16x16x32_bf16 v[122:125], v[138:141], v[172:175], v[122:125]
	v_mfma_f32_16x16x32_bf16 v[114:117], v[130:133], v[180:183], v[114:117]
	v_mfma_f32_16x16x32_bf16 v[106:109], v[138:141], v[180:183], v[106:109]
	v_mfma_f32_16x16x32_bf16 v[98:101], v[130:133], v[194:197], v[98:101]
	v_mfma_f32_16x16x32_bf16 v[90:93], v[138:141], v[194:197], v[90:93]
	v_mfma_f32_16x16x32_bf16 v[82:85], v[130:133], v[202:205], v[82:85]
	v_mfma_f32_16x16x32_bf16 v[74:77], v[138:141], v[202:205], v[74:77]
	v_mfma_f32_16x16x32_bf16 v[126:129], v[134:137], v[176:179], v[126:129]
	v_mfma_f32_16x16x32_bf16 v[122:125], v[142:145], v[176:179], v[122:125]
	v_mfma_f32_16x16x32_bf16 v[114:117], v[134:137], v[190:193], v[114:117]
	v_mfma_f32_16x16x32_bf16 v[106:109], v[142:145], v[190:193], v[106:109]
	v_mfma_f32_16x16x32_bf16 v[98:101], v[134:137], v[198:201], v[98:101]
	v_mfma_f32_16x16x32_bf16 v[90:93], v[142:145], v[198:201], v[90:93]
	v_mfma_f32_16x16x32_bf16 v[82:85], v[134:137], v[206:209], v[82:85]
	v_mfma_f32_16x16x32_bf16 v[74:77], v[142:145], v[206:209], v[74:77]
	s_setprio 0
	s_setprio 1
	v_mfma_f32_16x16x32_bf16 v[118:121], v[146:149], v[172:175], v[118:121]
	v_mfma_f32_16x16x32_bf16 v[110:113], v[154:157], v[172:175], v[110:113]
	v_mfma_f32_16x16x32_bf16 v[102:105], v[146:149], v[180:183], v[102:105]
	v_mfma_f32_16x16x32_bf16 v[94:97], v[154:157], v[180:183], v[94:97]
	v_mfma_f32_16x16x32_bf16 v[86:89], v[146:149], v[194:197], v[86:89]
	v_mfma_f32_16x16x32_bf16 v[78:81], v[154:157], v[194:197], v[78:81]
	v_mfma_f32_16x16x32_bf16 v[70:73], v[146:149], v[202:205], v[70:73]
	v_mfma_f32_16x16x32_bf16 v[66:69], v[154:157], v[202:205], v[66:69]
	v_mfma_f32_16x16x32_bf16 v[118:121], v[150:153], v[176:179], v[118:121]
	v_mfma_f32_16x16x32_bf16 v[110:113], v[168:171], v[176:179], v[110:113]
	v_mfma_f32_16x16x32_bf16 v[102:105], v[150:153], v[190:193], v[102:105]
	v_mfma_f32_16x16x32_bf16 v[94:97], v[168:171], v[190:193], v[94:97]
	v_mfma_f32_16x16x32_bf16 v[86:89], v[150:153], v[198:201], v[86:89]
	v_mfma_f32_16x16x32_bf16 v[78:81], v[168:171], v[198:201], v[78:81]
	v_mfma_f32_16x16x32_bf16 v[70:73], v[150:153], v[206:209], v[70:73]
	v_mfma_f32_16x16x32_bf16 v[66:69], v[168:171], v[206:209], v[66:69]
	s_setprio 0
	s_barrier
	s_add_i32 s43, s43, s44
	v_lshl_add_u64 v[216:217], s[28:29], 0, v[0:1]
	s_mov_b32 m0, s43
	ds_read_b128 v[172:175], v188 offset:16384
	ds_read_b128 v[176:179], v188 offset:17408
	ds_read_b128 v[180:183], v188 offset:18432
	ds_read_b128 v[190:193], v188 offset:19456
	ds_read_b128 v[194:197], v188 offset:20480
	ds_read_b128 v[198:201], v188 offset:21504
	ds_read_b128 v[202:205], v188 offset:22528
	ds_read_b128 v[206:209], v188 offset:23552
	global_load_lds_dwordx4 v[216:217], off
	s_add_i32 m0, s43, 0x2000
	s_add_u32 s58, s28, 0x40000
	v_lshl_add_u64 v[218:219], s[28:29], 0, v[158:159]
	s_addc_u32 s59, s29, 0
	s_add_i32 s43, s63, s44
	global_load_lds_dwordx4 v[218:219], off
	v_lshl_add_u64 v[220:221], s[58:59], 0, v[0:1]
	s_mov_b32 m0, s43
	v_lshl_add_u64 v[222:223], s[30:31], 0, v[160:161]
	global_load_lds_dwordx4 v[220:221], off
	v_lshl_add_u64 v[220:221], s[58:59], 0, v[158:159]
	s_add_i32 m0, s43, 0x2000
	s_nop 0
	global_load_lds_dwordx4 v[220:221], off
	v_lshl_add_u64 v[220:221], s[30:31], 0, v[162:163]
	s_mov_b32 m0, s45
	s_nop 0
	global_load_lds_dwordx4 v[220:221], off
	s_mov_b32 m0, s46
	s_nop 0
	global_load_lds_dwordx4 v[222:223], off
	s_waitcnt vmcnt(8)
	s_waitcnt lgkmcnt(0)
	s_barrier
	s_setprio 1
	s_waitcnt lgkmcnt(0)
	v_mfma_f32_16x16x32_bf16 v[62:65], v[130:133], v[172:175], v[62:65]
	v_mfma_f32_16x16x32_bf16 v[58:61], v[138:141], v[172:175], v[58:61]
	v_mfma_f32_16x16x32_bf16 v[50:53], v[130:133], v[180:183], v[50:53]
	v_mfma_f32_16x16x32_bf16 v[42:45], v[138:141], v[180:183], v[42:45]
	v_mfma_f32_16x16x32_bf16 v[34:37], v[130:133], v[194:197], v[34:37]
	v_mfma_f32_16x16x32_bf16 v[26:29], v[138:141], v[194:197], v[26:29]
	v_mfma_f32_16x16x32_bf16 v[18:21], v[130:133], v[202:205], v[18:21]
	v_mfma_f32_16x16x32_bf16 v[10:13], v[138:141], v[202:205], v[10:13]
	v_mfma_f32_16x16x32_bf16 v[62:65], v[134:137], v[176:179], v[62:65]
	v_mfma_f32_16x16x32_bf16 v[58:61], v[142:145], v[176:179], v[58:61]
	v_mfma_f32_16x16x32_bf16 v[50:53], v[134:137], v[190:193], v[50:53]
	v_mfma_f32_16x16x32_bf16 v[42:45], v[142:145], v[190:193], v[42:45]
	v_mfma_f32_16x16x32_bf16 v[34:37], v[134:137], v[198:201], v[34:37]
	v_mfma_f32_16x16x32_bf16 v[26:29], v[142:145], v[198:201], v[26:29]
	v_mfma_f32_16x16x32_bf16 v[18:21], v[134:137], v[206:209], v[18:21]
	v_mfma_f32_16x16x32_bf16 v[10:13], v[142:145], v[206:209], v[10:13]
	s_setprio 0
	s_setprio 1
	v_mfma_f32_16x16x32_bf16 v[54:57], v[146:149], v[172:175], v[54:57]
	v_mfma_f32_16x16x32_bf16 v[46:49], v[154:157], v[172:175], v[46:49]
	v_mfma_f32_16x16x32_bf16 v[38:41], v[146:149], v[180:183], v[38:41]
	v_mfma_f32_16x16x32_bf16 v[30:33], v[154:157], v[180:183], v[30:33]
	v_mfma_f32_16x16x32_bf16 v[22:25], v[146:149], v[194:197], v[22:25]
	v_mfma_f32_16x16x32_bf16 v[14:17], v[154:157], v[194:197], v[14:17]
	v_mfma_f32_16x16x32_bf16 v[6:9], v[146:149], v[202:205], v[6:9]
	v_mfma_f32_16x16x32_bf16 v[2:5], v[154:157], v[202:205], v[2:5]
	v_mfma_f32_16x16x32_bf16 v[54:57], v[150:153], v[176:179], v[54:57]
	v_mfma_f32_16x16x32_bf16 v[46:49], v[168:171], v[176:179], v[46:49]
	v_mfma_f32_16x16x32_bf16 v[38:41], v[150:153], v[190:193], v[38:41]
	v_mfma_f32_16x16x32_bf16 v[30:33], v[168:171], v[190:193], v[30:33]
	v_mfma_f32_16x16x32_bf16 v[22:25], v[150:153], v[198:201], v[22:25]
	v_mfma_f32_16x16x32_bf16 v[14:17], v[168:171], v[198:201], v[14:17]
	v_mfma_f32_16x16x32_bf16 v[6:9], v[150:153], v[206:209], v[6:9]
	v_mfma_f32_16x16x32_bf16 v[2:5], v[168:171], v[206:209], v[2:5]
	s_setprio 0
	s_barrier
	s_add_i32 s43, 0, 0x18000
	s_add_i32 s58, 0, 0x1c000
	v_add_u32_e32 v142, s43, v186
	v_add_u32_e32 v168, s58, v186
	ds_read_b128 v[130:133], v142
	ds_read_b128 v[134:137], v142 offset:1024
	ds_read_b128 v[138:141], v142 offset:2048
	ds_read_b128 v[142:145], v142 offset:3072
	ds_read_b128 v[146:149], v168
	ds_read_b128 v[150:153], v168 offset:1024
	ds_read_b128 v[154:157], v168 offset:2048
	ds_read_b128 v[168:171], v168 offset:3072
	s_add_u32 s30, s30, 0x40000
	s_addc_u32 s31, s31, 0
	s_mov_b32 m0, s47
	v_lshl_add_u64 v[224:225], s[30:31], 0, v[162:163]
	ds_read_b128 v[172:175], v188 offset:32768
	ds_read_b128 v[176:179], v188 offset:33792
	ds_read_b128 v[180:183], v188 offset:34816
	ds_read_b128 v[190:193], v188 offset:35840
	ds_read_b128 v[194:197], v188 offset:36864
	ds_read_b128 v[198:201], v188 offset:37888
	ds_read_b128 v[202:205], v188 offset:38912
	ds_read_b128 v[206:209], v188 offset:39936
	global_load_lds_dwordx4 v[224:225], off
	v_lshl_add_u64 v[224:225], s[30:31], 0, v[160:161]
	s_mov_b32 m0, s48
	s_nop 0
	global_load_lds_dwordx4 v[224:225], off
	s_waitcnt vmcnt(8)
	s_waitcnt lgkmcnt(0)
	s_barrier
	s_setprio 1
	s_waitcnt lgkmcnt(0)
	v_mfma_f32_16x16x32_bf16 v[126:129], v[130:133], v[172:175], v[126:129]
	v_mfma_f32_16x16x32_bf16 v[122:125], v[138:141], v[172:175], v[122:125]
	v_mfma_f32_16x16x32_bf16 v[114:117], v[130:133], v[180:183], v[114:117]
	v_mfma_f32_16x16x32_bf16 v[106:109], v[138:141], v[180:183], v[106:109]
	v_mfma_f32_16x16x32_bf16 v[98:101], v[130:133], v[194:197], v[98:101]
	v_mfma_f32_16x16x32_bf16 v[90:93], v[138:141], v[194:197], v[90:93]
	v_mfma_f32_16x16x32_bf16 v[82:85], v[130:133], v[202:205], v[82:85]
	v_mfma_f32_16x16x32_bf16 v[74:77], v[138:141], v[202:205], v[74:77]
	v_mfma_f32_16x16x32_bf16 v[126:129], v[134:137], v[176:179], v[126:129]
	v_mfma_f32_16x16x32_bf16 v[122:125], v[142:145], v[176:179], v[122:125]
	v_mfma_f32_16x16x32_bf16 v[114:117], v[134:137], v[190:193], v[114:117]
	v_mfma_f32_16x16x32_bf16 v[106:109], v[142:145], v[190:193], v[106:109]
	v_mfma_f32_16x16x32_bf16 v[98:101], v[134:137], v[198:201], v[98:101]
	v_mfma_f32_16x16x32_bf16 v[90:93], v[142:145], v[198:201], v[90:93]
	v_mfma_f32_16x16x32_bf16 v[82:85], v[134:137], v[206:209], v[82:85]
	v_mfma_f32_16x16x32_bf16 v[74:77], v[142:145], v[206:209], v[74:77]
	s_setprio 0
	s_setprio 1
	v_mfma_f32_16x16x32_bf16 v[118:121], v[146:149], v[172:175], v[118:121]
	v_mfma_f32_16x16x32_bf16 v[110:113], v[154:157], v[172:175], v[110:113]
	v_mfma_f32_16x16x32_bf16 v[102:105], v[146:149], v[180:183], v[102:105]
	v_mfma_f32_16x16x32_bf16 v[94:97], v[154:157], v[180:183], v[94:97]
	v_mfma_f32_16x16x32_bf16 v[86:89], v[146:149], v[194:197], v[86:89]
	v_mfma_f32_16x16x32_bf16 v[78:81], v[154:157], v[194:197], v[78:81]
	v_mfma_f32_16x16x32_bf16 v[70:73], v[146:149], v[202:205], v[70:73]
	v_mfma_f32_16x16x32_bf16 v[66:69], v[154:157], v[202:205], v[66:69]
	v_mfma_f32_16x16x32_bf16 v[118:121], v[150:153], v[176:179], v[118:121]
	v_mfma_f32_16x16x32_bf16 v[110:113], v[168:171], v[176:179], v[110:113]
	v_mfma_f32_16x16x32_bf16 v[102:105], v[150:153], v[190:193], v[102:105]
	v_mfma_f32_16x16x32_bf16 v[94:97], v[168:171], v[190:193], v[94:97]
	v_mfma_f32_16x16x32_bf16 v[86:89], v[150:153], v[198:201], v[86:89]
	v_mfma_f32_16x16x32_bf16 v[78:81], v[168:171], v[198:201], v[78:81]
	v_mfma_f32_16x16x32_bf16 v[70:73], v[150:153], v[206:209], v[70:73]
	v_mfma_f32_16x16x32_bf16 v[66:69], v[168:171], v[206:209], v[66:69]
	s_setprio 0
	s_barrier
	s_add_i32 s30, s43, s44
	v_lshl_add_u64 v[216:217], v[216:217], 0, s[56:57]
	s_mov_b32 m0, s30
	ds_read_b128 v[172:175], v188 offset:49152
	ds_read_b128 v[176:179], v188 offset:50176
	ds_read_b128 v[180:183], v188 offset:51200
	ds_read_b128 v[190:193], v188 offset:52224
	ds_read_b128 v[194:197], v188 offset:53248
	ds_read_b128 v[198:201], v188 offset:54272
	ds_read_b128 v[202:205], v188 offset:55296
	ds_read_b128 v[206:209], v188 offset:56320
	global_load_lds_dwordx4 v[216:217], off
	s_add_i32 m0, s30, 0x2000
	s_add_u32 s28, s28, 0x40080
	v_lshl_add_u64 v[216:217], v[218:219], 0, s[56:57]
	s_addc_u32 s29, s29, 0
	s_add_i32 s30, s58, s44
	global_load_lds_dwordx4 v[216:217], off
	v_lshl_add_u64 v[216:217], s[28:29], 0, v[0:1]
	s_mov_b32 m0, s30
	s_nop 0
	global_load_lds_dwordx4 v[216:217], off
	v_lshl_add_u64 v[216:217], s[28:29], 0, v[158:159]
	s_add_i32 m0, s30, 0x2000
	s_nop 0
	global_load_lds_dwordx4 v[216:217], off
	v_lshl_add_u64 v[216:217], v[220:221], 0, s[56:57]
	s_mov_b32 m0, s49
	s_nop 0
	global_load_lds_dwordx4 v[216:217], off
	v_lshl_add_u64 v[216:217], v[222:223], 0, s[56:57]
	s_mov_b32 m0, s52
	s_nop 0
	global_load_lds_dwordx4 v[216:217], off
	s_waitcnt vmcnt(8)
	s_waitcnt lgkmcnt(0)
	s_barrier
	s_setprio 1
	s_waitcnt lgkmcnt(0)
	v_mfma_f32_16x16x32_bf16 v[62:65], v[130:133], v[172:175], v[62:65]
	v_mfma_f32_16x16x32_bf16 v[58:61], v[138:141], v[172:175], v[58:61]
	v_mfma_f32_16x16x32_bf16 v[50:53], v[130:133], v[180:183], v[50:53]
	v_mfma_f32_16x16x32_bf16 v[42:45], v[138:141], v[180:183], v[42:45]
	v_mfma_f32_16x16x32_bf16 v[34:37], v[130:133], v[194:197], v[34:37]
	v_mfma_f32_16x16x32_bf16 v[26:29], v[138:141], v[194:197], v[26:29]
	v_mfma_f32_16x16x32_bf16 v[18:21], v[130:133], v[202:205], v[18:21]
	v_mfma_f32_16x16x32_bf16 v[10:13], v[138:141], v[202:205], v[10:13]
	v_mfma_f32_16x16x32_bf16 v[62:65], v[134:137], v[176:179], v[62:65]
	v_mfma_f32_16x16x32_bf16 v[58:61], v[142:145], v[176:179], v[58:61]
	v_mfma_f32_16x16x32_bf16 v[50:53], v[134:137], v[190:193], v[50:53]
	v_mfma_f32_16x16x32_bf16 v[42:45], v[142:145], v[190:193], v[42:45]
	v_mfma_f32_16x16x32_bf16 v[34:37], v[134:137], v[198:201], v[34:37]
	v_mfma_f32_16x16x32_bf16 v[26:29], v[142:145], v[198:201], v[26:29]
	v_mfma_f32_16x16x32_bf16 v[18:21], v[134:137], v[206:209], v[18:21]
	v_mfma_f32_16x16x32_bf16 v[10:13], v[142:145], v[206:209], v[10:13]
	s_setprio 0
	s_setprio 1
	v_mfma_f32_16x16x32_bf16 v[54:57], v[146:149], v[172:175], v[54:57]
	v_mfma_f32_16x16x32_bf16 v[46:49], v[154:157], v[172:175], v[46:49]
	v_mfma_f32_16x16x32_bf16 v[38:41], v[146:149], v[180:183], v[38:41]
	v_mfma_f32_16x16x32_bf16 v[30:33], v[154:157], v[180:183], v[30:33]
	v_mfma_f32_16x16x32_bf16 v[22:25], v[146:149], v[194:197], v[22:25]
	v_mfma_f32_16x16x32_bf16 v[14:17], v[154:157], v[194:197], v[14:17]
	v_mfma_f32_16x16x32_bf16 v[6:9], v[146:149], v[202:205], v[6:9]
	v_mfma_f32_16x16x32_bf16 v[2:5], v[154:157], v[202:205], v[2:5]
	v_mfma_f32_16x16x32_bf16 v[54:57], v[150:153], v[176:179], v[54:57]
	v_mfma_f32_16x16x32_bf16 v[46:49], v[168:171], v[176:179], v[46:49]
	v_mfma_f32_16x16x32_bf16 v[38:41], v[150:153], v[190:193], v[38:41]
	v_mfma_f32_16x16x32_bf16 v[30:33], v[168:171], v[190:193], v[30:33]
	v_mfma_f32_16x16x32_bf16 v[22:25], v[150:153], v[198:201], v[22:25]
	v_mfma_f32_16x16x32_bf16 v[14:17], v[168:171], v[198:201], v[14:17]
	v_mfma_f32_16x16x32_bf16 v[6:9], v[150:153], v[206:209], v[6:9]
	v_mfma_f32_16x16x32_bf16 v[2:5], v[168:171], v[206:209], v[2:5]
	s_setprio 0
	s_barrier
	s_add_i32 s42, s42, 2
	s_add_u32 s23, s23, 0x100
	s_addc_u32 s33, s33, 0
	s_add_u32 s6, s6, 0x100
	s_addc_u32 s7, s7, 0
	s_cmp_gt_u32 s42, 13
	s_cbranch_scc0 .LBB0_417
	s_and_b64 vcc, exec, s[18:19]
	s_cbranch_vccz .LBB0_420
	s_barrier
.LBB0_420:
	v_mov_b32_e32 v200, 0
	v_mov_b32_e32 v201, 0
	v_mov_b32_e32 v202, 0
	v_mov_b32_e32 v203, 0
	v_lshl_add_u32 v182, s4, 8, v185
	s_cmp_gt_u32 s62, 3
	s_cselect_b64 s[4:5], -1, 0
	v_cndmask_b32_e64 v190, v230, 1.0, s[4:5]
	s_waitcnt vmcnt(8)
	v_add_f32_e32 v240, v240, v241
	v_add_f32_e32 v242, v242, v243
	v_add_f32_e32 v240, v240, v242
	v_fmamk_f32 v240, v240, 0x3a800000, v226
	v_rsq_f32_e32 v240, v240
	v_add_f32_e32 v244, v244, v245
	v_add_f32_e32 v184, v184, v189
	v_add_f32_e32 v244, v244, v184
	v_fmamk_f32 v244, v244, 0x3a800000, v226
	v_rsq_f32_e32 v244, v244
	v_and_b32_e32 v191, 15, v185
	v_lshlrev_b32_e32 v191, 2, v191
	v_add_u32_e32 v192, 64, v191
	v_add_u32_e32 v193, 0x80, v191
	v_add_u32_e32 v194, 0xc0, v191
	v_mul_f32_e32 v240, v240, v190
	v_mul_f32_e32 v244, v244, v190
	ds_bpermute_b32 v144, v191, v240
	ds_bpermute_b32 v146, v191, v244
	ds_bpermute_b32 v148, v192, v240
	ds_bpermute_b32 v150, v192, v244
	ds_bpermute_b32 v152, v193, v240
	ds_bpermute_b32 v154, v193, v244
	ds_bpermute_b32 v156, v194, v240
	ds_bpermute_b32 v168, v194, v244
	v_lshl_or_b32 v170, s62, 8, v187
	v_lshlrev_b32_e32 v170, 1, v170
	v_mov_b32_e32 v171, 0
	v_mov_b64_e32 v[172:173], s[14:15]
	v_mad_i64_i32 v[172:173], s[4:5], v182, s69, v[172:173]
	v_lshl_add_u64 v[172:173], v[172:173], 0, v[170:171]
	s_waitcnt lgkmcnt(0)
	v_pk_mul_f32 v[126:127], v[126:127], v[144:145] op_sel_hi:[1,0]
	v_pk_mul_f32 v[128:129], v[128:129], v[144:145] op_sel_hi:[1,0]
	v_pk_mul_f32 v[122:123], v[122:123], v[144:145] op_sel_hi:[1,0]
	v_pk_mul_f32 v[124:125], v[124:125], v[144:145] op_sel_hi:[1,0]
	v_cvt_pk_bf16_f32 v126, v126, v127
	v_cvt_pk_bf16_f32 v127, v128, v129
	v_cvt_pk_bf16_f32 v128, v122, v123
	v_cvt_pk_bf16_f32 v129, v124, v125
	global_store_dwordx4 v[172:173], v[126:129], off
	v_pk_mul_f32 v[118:119], v[118:119], v[144:145] op_sel_hi:[1,0]
	v_pk_mul_f32 v[120:121], v[120:121], v[144:145] op_sel_hi:[1,0]
	v_pk_mul_f32 v[110:111], v[110:111], v[144:145] op_sel_hi:[1,0]
	v_pk_mul_f32 v[112:113], v[112:113], v[144:145] op_sel_hi:[1,0]
	v_cvt_pk_bf16_f32 v118, v118, v119
	v_cvt_pk_bf16_f32 v119, v120, v121
	v_cvt_pk_bf16_f32 v120, v110, v111
	v_cvt_pk_bf16_f32 v121, v112, v113
	global_store_dwordx4 v[172:173], v[118:121], off offset:256
	s_mov_b64 s[42:43], 0xa000
	v_lshl_add_u64 v[176:177], v[172:173], 0, s[42:43]
	v_pk_mul_f32 v[114:115], v[114:115], v[146:147] op_sel_hi:[1,0]
	v_pk_mul_f32 v[116:117], v[116:117], v[146:147] op_sel_hi:[1,0]
	v_pk_mul_f32 v[106:107], v[106:107], v[146:147] op_sel_hi:[1,0]
	v_pk_mul_f32 v[108:109], v[108:109], v[146:147] op_sel_hi:[1,0]
	v_cvt_pk_bf16_f32 v114, v114, v115
	v_cvt_pk_bf16_f32 v115, v116, v117
	v_cvt_pk_bf16_f32 v116, v106, v107
	v_cvt_pk_bf16_f32 v117, v108, v109
	global_store_dwordx4 v[176:177], v[114:117], off
	v_pk_mul_f32 v[102:103], v[102:103], v[146:147] op_sel_hi:[1,0]
	v_pk_mul_f32 v[104:105], v[104:105], v[146:147] op_sel_hi:[1,0]
	v_pk_mul_f32 v[94:95], v[94:95], v[146:147] op_sel_hi:[1,0]
	v_pk_mul_f32 v[96:97], v[96:97], v[146:147] op_sel_hi:[1,0]
	v_cvt_pk_bf16_f32 v102, v102, v103
	v_cvt_pk_bf16_f32 v103, v104, v105
	v_cvt_pk_bf16_f32 v104, v94, v95
	v_cvt_pk_bf16_f32 v105, v96, v97
	global_store_dwordx4 v[176:177], v[102:105], off offset:256
	s_mov_b64 s[42:43], 0x14000
	v_lshl_add_u64 v[174:175], v[172:173], 0, s[42:43]
	v_pk_mul_f32 v[98:99], v[98:99], v[148:149] op_sel_hi:[1,0]
	v_pk_mul_f32 v[100:101], v[100:101], v[148:149] op_sel_hi:[1,0]
	v_pk_mul_f32 v[90:91], v[90:91], v[148:149] op_sel_hi:[1,0]
	v_pk_mul_f32 v[92:93], v[92:93], v[148:149] op_sel_hi:[1,0]
	v_cvt_pk_bf16_f32 v98, v98, v99
	v_cvt_pk_bf16_f32 v99, v100, v101
	v_cvt_pk_bf16_f32 v100, v90, v91
	v_cvt_pk_bf16_f32 v101, v92, v93
	global_store_dwordx4 v[174:175], v[98:101], off
	v_pk_mul_f32 v[86:87], v[86:87], v[148:149] op_sel_hi:[1,0]
	v_pk_mul_f32 v[88:89], v[88:89], v[148:149] op_sel_hi:[1,0]
	v_pk_mul_f32 v[78:79], v[78:79], v[148:149] op_sel_hi:[1,0]
	v_pk_mul_f32 v[80:81], v[80:81], v[148:149] op_sel_hi:[1,0]
	v_cvt_pk_bf16_f32 v86, v86, v87
	v_cvt_pk_bf16_f32 v87, v88, v89
	v_cvt_pk_bf16_f32 v88, v78, v79
	v_cvt_pk_bf16_f32 v89, v80, v81
	global_store_dwordx4 v[174:175], v[86:89], off offset:256
	s_mov_b64 s[42:43], 0x1e000
	v_lshl_add_u64 v[176:177], v[172:173], 0, s[42:43]
	v_pk_mul_f32 v[82:83], v[82:83], v[150:151] op_sel_hi:[1,0]
	v_pk_mul_f32 v[84:85], v[84:85], v[150:151] op_sel_hi:[1,0]
	v_pk_mul_f32 v[74:75], v[74:75], v[150:151] op_sel_hi:[1,0]
	v_pk_mul_f32 v[76:77], v[76:77], v[150:151] op_sel_hi:[1,0]
	v_cvt_pk_bf16_f32 v82, v82, v83
	v_cvt_pk_bf16_f32 v83, v84, v85
	v_cvt_pk_bf16_f32 v84, v74, v75
	v_cvt_pk_bf16_f32 v85, v76, v77
	global_store_dwordx4 v[176:177], v[82:85], off
	v_pk_mul_f32 v[70:71], v[70:71], v[150:151] op_sel_hi:[1,0]
	v_pk_mul_f32 v[72:73], v[72:73], v[150:151] op_sel_hi:[1,0]
	v_pk_mul_f32 v[66:67], v[66:67], v[150:151] op_sel_hi:[1,0]
	v_pk_mul_f32 v[68:69], v[68:69], v[150:151] op_sel_hi:[1,0]
	v_cvt_pk_bf16_f32 v70, v70, v71
	v_cvt_pk_bf16_f32 v71, v72, v73
	v_cvt_pk_bf16_f32 v72, v66, v67
	v_cvt_pk_bf16_f32 v73, v68, v69
	global_store_dwordx4 v[176:177], v[70:73], off offset:256
	s_mov_b64 s[42:43], 0x50000
	v_lshl_add_u64 v[174:175], v[172:173], 0, s[42:43]
	v_pk_mul_f32 v[62:63], v[62:63], v[152:153] op_sel_hi:[1,0]
	v_pk_mul_f32 v[64:65], v[64:65], v[152:153] op_sel_hi:[1,0]
	v_pk_mul_f32 v[58:59], v[58:59], v[152:153] op_sel_hi:[1,0]
	v_pk_mul_f32 v[60:61], v[60:61], v[152:153] op_sel_hi:[1,0]
	v_cvt_pk_bf16_f32 v62, v62, v63
	v_cvt_pk_bf16_f32 v63, v64, v65
	v_cvt_pk_bf16_f32 v64, v58, v59
	v_cvt_pk_bf16_f32 v65, v60, v61
	global_store_dwordx4 v[174:175], v[62:65], off
	v_pk_mul_f32 v[54:55], v[54:55], v[152:153] op_sel_hi:[1,0]
	v_pk_mul_f32 v[56:57], v[56:57], v[152:153] op_sel_hi:[1,0]
	v_pk_mul_f32 v[46:47], v[46:47], v[152:153] op_sel_hi:[1,0]
	v_pk_mul_f32 v[48:49], v[48:49], v[152:153] op_sel_hi:[1,0]
	v_cvt_pk_bf16_f32 v54, v54, v55
	v_cvt_pk_bf16_f32 v55, v56, v57
	v_cvt_pk_bf16_f32 v56, v46, v47
	v_cvt_pk_bf16_f32 v57, v48, v49
	global_store_dwordx4 v[174:175], v[54:57], off offset:256
	s_mov_b64 s[42:43], 0x5a000
	v_lshl_add_u64 v[176:177], v[172:173], 0, s[42:43]
	v_pk_mul_f32 v[50:51], v[50:51], v[154:155] op_sel_hi:[1,0]
	v_pk_mul_f32 v[52:53], v[52:53], v[154:155] op_sel_hi:[1,0]
	v_pk_mul_f32 v[42:43], v[42:43], v[154:155] op_sel_hi:[1,0]
	v_pk_mul_f32 v[44:45], v[44:45], v[154:155] op_sel_hi:[1,0]
	v_cvt_pk_bf16_f32 v50, v50, v51
	v_cvt_pk_bf16_f32 v51, v52, v53
	v_cvt_pk_bf16_f32 v52, v42, v43
	v_cvt_pk_bf16_f32 v53, v44, v45
	global_store_dwordx4 v[176:177], v[50:53], off
	v_pk_mul_f32 v[38:39], v[38:39], v[154:155] op_sel_hi:[1,0]
	v_pk_mul_f32 v[40:41], v[40:41], v[154:155] op_sel_hi:[1,0]
	v_pk_mul_f32 v[30:31], v[30:31], v[154:155] op_sel_hi:[1,0]
	v_pk_mul_f32 v[32:33], v[32:33], v[154:155] op_sel_hi:[1,0]
	v_cvt_pk_bf16_f32 v38, v38, v39
	v_cvt_pk_bf16_f32 v39, v40, v41
	v_cvt_pk_bf16_f32 v40, v30, v31
	v_cvt_pk_bf16_f32 v41, v32, v33
	global_store_dwordx4 v[176:177], v[38:41], off offset:256
	s_mov_b64 s[42:43], 0x64000
	v_lshl_add_u64 v[174:175], v[172:173], 0, s[42:43]
	v_pk_mul_f32 v[34:35], v[34:35], v[156:157] op_sel_hi:[1,0]
	v_pk_mul_f32 v[36:37], v[36:37], v[156:157] op_sel_hi:[1,0]
	v_pk_mul_f32 v[26:27], v[26:27], v[156:157] op_sel_hi:[1,0]
	v_pk_mul_f32 v[28:29], v[28:29], v[156:157] op_sel_hi:[1,0]
	v_cvt_pk_bf16_f32 v34, v34, v35
	v_cvt_pk_bf16_f32 v35, v36, v37
	v_cvt_pk_bf16_f32 v36, v26, v27
	v_cvt_pk_bf16_f32 v37, v28, v29
	global_store_dwordx4 v[174:175], v[34:37], off
	v_pk_mul_f32 v[22:23], v[22:23], v[156:157] op_sel_hi:[1,0]
	v_pk_mul_f32 v[24:25], v[24:25], v[156:157] op_sel_hi:[1,0]
	v_pk_mul_f32 v[14:15], v[14:15], v[156:157] op_sel_hi:[1,0]
	v_pk_mul_f32 v[16:17], v[16:17], v[156:157] op_sel_hi:[1,0]
	v_cvt_pk_bf16_f32 v22, v22, v23
	v_cvt_pk_bf16_f32 v23, v24, v25
	v_cvt_pk_bf16_f32 v24, v14, v15
	v_cvt_pk_bf16_f32 v25, v16, v17
	global_store_dwordx4 v[174:175], v[22:25], off offset:256
	s_mov_b64 s[42:43], 0x6e000
	v_lshl_add_u64 v[176:177], v[172:173], 0, s[42:43]
	v_pk_mul_f32 v[18:19], v[18:19], v[168:169] op_sel_hi:[1,0]
	v_pk_mul_f32 v[20:21], v[20:21], v[168:169] op_sel_hi:[1,0]
	v_pk_mul_f32 v[10:11], v[10:11], v[168:169] op_sel_hi:[1,0]
	v_pk_mul_f32 v[12:13], v[12:13], v[168:169] op_sel_hi:[1,0]
	v_cvt_pk_bf16_f32 v18, v18, v19
	v_cvt_pk_bf16_f32 v19, v20, v21
	v_cvt_pk_bf16_f32 v20, v10, v11
	v_cvt_pk_bf16_f32 v21, v12, v13
	global_store_dwordx4 v[176:177], v[18:21], off
	v_pk_mul_f32 v[6:7], v[6:7], v[168:169] op_sel_hi:[1,0]
	v_pk_mul_f32 v[8:9], v[8:9], v[168:169] op_sel_hi:[1,0]
	v_pk_mul_f32 v[2:3], v[2:3], v[168:169] op_sel_hi:[1,0]
	v_pk_mul_f32 v[4:5], v[4:5], v[168:169] op_sel_hi:[1,0]
	v_cvt_pk_bf16_f32 v6, v6, v7
	v_cvt_pk_bf16_f32 v7, v8, v9
	v_cvt_pk_bf16_f32 v8, v2, v3
	v_cvt_pk_bf16_f32 v9, v4, v5
	global_store_dwordx4 v[176:177], v[6:9], off offset:256
	s_nop 3
	v_mfma_f32_32x32x16_bf16 v[2:17], v[200:203], v[200:203], 0
	v_mfma_f32_32x32x16_bf16 v[18:33], v[200:203], v[200:203], 0
	v_mfma_f32_32x32x16_bf16 v[34:49], v[200:203], v[200:203], 0
	v_mfma_f32_32x32x16_bf16 v[50:65], v[200:203], v[200:203], 0
	v_mfma_f32_32x32x16_bf16 v[66:81], v[200:203], v[200:203], 0
	v_mfma_f32_32x32x16_bf16 v[82:97], v[200:203], v[200:203], 0
	v_mfma_f32_32x32x16_bf16 v[98:113], v[200:203], v[200:203], 0
	v_mfma_f32_32x32x16_bf16 v[114:129], v[200:203], v[200:203], 0
	s_andn2_b64 vcc, exec, s[40:41]
	s_mov_b64 s[6:7], -1
	s_cbranch_vccnz .LBB0_413
	s_andn2_b64 vcc, exec, s[12:13]
	s_cbranch_vccnz .LBB0_412
	s_barrier
	s_branch .LBB0_412

.LBB0_839:
	v_mov_b32_e32 v200, 0
	v_mov_b32_e32 v201, 0
	v_mov_b32_e32 v202, 0
	v_mov_b32_e32 v203, 0
	v_lshl_add_u32 v182, s4, 8, v185
	s_lshl_b32 s4, 1, s52
	s_and_b32 s4, s4, 0x18f
	s_cmp_eq_u32 s4, 0
	s_cselect_b64 s[4:5], -1, 0
	v_cndmask_b32_e64 v190, v230, 1.0, s[4:5]
	s_waitcnt vmcnt(8)
	v_add_f32_e32 v240, v240, v241
	v_add_f32_e32 v242, v242, v243
	v_add_f32_e32 v240, v240, v242
	v_fmamk_f32 v240, v240, 0x3a800000, v226
	v_rsq_f32_e32 v240, v240
	v_add_f32_e32 v244, v244, v245
	v_add_f32_e32 v184, v184, v189
	v_add_f32_e32 v244, v244, v184
	v_fmamk_f32 v244, v244, 0x3a800000, v226
	v_rsq_f32_e32 v244, v244
	v_and_b32_e32 v191, 15, v185
	v_lshlrev_b32_e32 v191, 2, v191
	v_add_u32_e32 v192, 64, v191
	v_add_u32_e32 v193, 0x80, v191
	v_add_u32_e32 v194, 0xc0, v191
	v_mul_f32_e32 v240, v240, v190
	v_mul_f32_e32 v244, v244, v190
	ds_bpermute_b32 v144, v191, v240
	ds_bpermute_b32 v146, v191, v244
	ds_bpermute_b32 v148, v192, v240
	ds_bpermute_b32 v150, v192, v244
	ds_bpermute_b32 v152, v193, v240
	ds_bpermute_b32 v154, v193, v244
	ds_bpermute_b32 v156, v194, v240
	ds_bpermute_b32 v168, v194, v244
	s_movk_i32 s6, 0x1a00
	v_lshl_or_b32 v170, s52, 8, v187
	v_lshlrev_b32_e32 v170, 1, v170
	v_mov_b32_e32 v171, 0
	v_mov_b64_e32 v[172:173], s[14:15]
	v_mad_i64_i32 v[172:173], s[4:5], v182, s6, v[172:173]
	v_lshl_add_u64 v[172:173], v[172:173], 0, v[170:171]
	s_waitcnt lgkmcnt(0)
	v_pk_mul_f32 v[126:127], v[126:127], v[144:145] op_sel_hi:[1,0]
	v_pk_mul_f32 v[128:129], v[128:129], v[144:145] op_sel_hi:[1,0]
	v_pk_mul_f32 v[122:123], v[122:123], v[144:145] op_sel_hi:[1,0]
	v_pk_mul_f32 v[124:125], v[124:125], v[144:145] op_sel_hi:[1,0]
	v_cvt_pk_bf16_f32 v126, v126, v127
	v_cvt_pk_bf16_f32 v127, v128, v129
	v_cvt_pk_bf16_f32 v128, v122, v123
	v_cvt_pk_bf16_f32 v129, v124, v125
	global_store_dwordx4 v[172:173], v[126:129], off
	v_pk_mul_f32 v[118:119], v[118:119], v[144:145] op_sel_hi:[1,0]
	v_pk_mul_f32 v[120:121], v[120:121], v[144:145] op_sel_hi:[1,0]
	v_pk_mul_f32 v[110:111], v[110:111], v[144:145] op_sel_hi:[1,0]
	v_pk_mul_f32 v[112:113], v[112:113], v[144:145] op_sel_hi:[1,0]
	v_cvt_pk_bf16_f32 v118, v118, v119
	v_cvt_pk_bf16_f32 v119, v120, v121
	v_cvt_pk_bf16_f32 v120, v110, v111
	v_cvt_pk_bf16_f32 v121, v112, v113
	global_store_dwordx4 v[172:173], v[118:121], off offset:256
	s_mov_b64 s[40:41], 0x1a000
	v_lshl_add_u64 v[176:177], v[172:173], 0, s[40:41]
	v_pk_mul_f32 v[114:115], v[114:115], v[146:147] op_sel_hi:[1,0]
	v_pk_mul_f32 v[116:117], v[116:117], v[146:147] op_sel_hi:[1,0]
	v_pk_mul_f32 v[106:107], v[106:107], v[146:147] op_sel_hi:[1,0]
	v_pk_mul_f32 v[108:109], v[108:109], v[146:147] op_sel_hi:[1,0]
	v_cvt_pk_bf16_f32 v114, v114, v115
	v_cvt_pk_bf16_f32 v115, v116, v117
	v_cvt_pk_bf16_f32 v116, v106, v107
	v_cvt_pk_bf16_f32 v117, v108, v109
	global_store_dwordx4 v[176:177], v[114:117], off
	v_pk_mul_f32 v[102:103], v[102:103], v[146:147] op_sel_hi:[1,0]
	v_pk_mul_f32 v[104:105], v[104:105], v[146:147] op_sel_hi:[1,0]
	v_pk_mul_f32 v[94:95], v[94:95], v[146:147] op_sel_hi:[1,0]
	v_pk_mul_f32 v[96:97], v[96:97], v[146:147] op_sel_hi:[1,0]
	v_cvt_pk_bf16_f32 v102, v102, v103
	v_cvt_pk_bf16_f32 v103, v104, v105
	v_cvt_pk_bf16_f32 v104, v94, v95
	v_cvt_pk_bf16_f32 v105, v96, v97
	global_store_dwordx4 v[176:177], v[102:105], off offset:256
	s_mov_b64 s[40:41], 0x34000
	v_lshl_add_u64 v[174:175], v[172:173], 0, s[40:41]
	v_pk_mul_f32 v[98:99], v[98:99], v[148:149] op_sel_hi:[1,0]
	v_pk_mul_f32 v[100:101], v[100:101], v[148:149] op_sel_hi:[1,0]
	v_pk_mul_f32 v[90:91], v[90:91], v[148:149] op_sel_hi:[1,0]
	v_pk_mul_f32 v[92:93], v[92:93], v[148:149] op_sel_hi:[1,0]
	v_cvt_pk_bf16_f32 v98, v98, v99
	v_cvt_pk_bf16_f32 v99, v100, v101
	v_cvt_pk_bf16_f32 v100, v90, v91
	v_cvt_pk_bf16_f32 v101, v92, v93
	global_store_dwordx4 v[174:175], v[98:101], off
	v_pk_mul_f32 v[86:87], v[86:87], v[148:149] op_sel_hi:[1,0]
	v_pk_mul_f32 v[88:89], v[88:89], v[148:149] op_sel_hi:[1,0]
	v_pk_mul_f32 v[78:79], v[78:79], v[148:149] op_sel_hi:[1,0]
	v_pk_mul_f32 v[80:81], v[80:81], v[148:149] op_sel_hi:[1,0]
	v_cvt_pk_bf16_f32 v86, v86, v87
	v_cvt_pk_bf16_f32 v87, v88, v89
	v_cvt_pk_bf16_f32 v88, v78, v79
	v_cvt_pk_bf16_f32 v89, v80, v81
	global_store_dwordx4 v[174:175], v[86:89], off offset:256
	s_mov_b64 s[40:41], 0x4e000
	v_lshl_add_u64 v[176:177], v[172:173], 0, s[40:41]
	v_pk_mul_f32 v[82:83], v[82:83], v[150:151] op_sel_hi:[1,0]
	v_pk_mul_f32 v[84:85], v[84:85], v[150:151] op_sel_hi:[1,0]
	v_pk_mul_f32 v[74:75], v[74:75], v[150:151] op_sel_hi:[1,0]
	v_pk_mul_f32 v[76:77], v[76:77], v[150:151] op_sel_hi:[1,0]
	v_cvt_pk_bf16_f32 v82, v82, v83
	v_cvt_pk_bf16_f32 v83, v84, v85
	v_cvt_pk_bf16_f32 v84, v74, v75
	v_cvt_pk_bf16_f32 v85, v76, v77
	global_store_dwordx4 v[176:177], v[82:85], off
	v_pk_mul_f32 v[70:71], v[70:71], v[150:151] op_sel_hi:[1,0]
	v_pk_mul_f32 v[72:73], v[72:73], v[150:151] op_sel_hi:[1,0]
	v_pk_mul_f32 v[66:67], v[66:67], v[150:151] op_sel_hi:[1,0]
	v_pk_mul_f32 v[68:69], v[68:69], v[150:151] op_sel_hi:[1,0]
	v_cvt_pk_bf16_f32 v70, v70, v71
	v_cvt_pk_bf16_f32 v71, v72, v73
	v_cvt_pk_bf16_f32 v72, v66, v67
	v_cvt_pk_bf16_f32 v73, v68, v69
	global_store_dwordx4 v[176:177], v[70:73], off offset:256
	s_mov_b64 s[40:41], 0xd0000
	v_lshl_add_u64 v[174:175], v[172:173], 0, s[40:41]
	v_pk_mul_f32 v[62:63], v[62:63], v[152:153] op_sel_hi:[1,0]
	v_pk_mul_f32 v[64:65], v[64:65], v[152:153] op_sel_hi:[1,0]
	v_pk_mul_f32 v[58:59], v[58:59], v[152:153] op_sel_hi:[1,0]
	v_pk_mul_f32 v[60:61], v[60:61], v[152:153] op_sel_hi:[1,0]
	v_cvt_pk_bf16_f32 v62, v62, v63
	v_cvt_pk_bf16_f32 v63, v64, v65
	v_cvt_pk_bf16_f32 v64, v58, v59
	v_cvt_pk_bf16_f32 v65, v60, v61
	global_store_dwordx4 v[174:175], v[62:65], off
	v_pk_mul_f32 v[54:55], v[54:55], v[152:153] op_sel_hi:[1,0]
	v_pk_mul_f32 v[56:57], v[56:57], v[152:153] op_sel_hi:[1,0]
	v_pk_mul_f32 v[46:47], v[46:47], v[152:153] op_sel_hi:[1,0]
	v_pk_mul_f32 v[48:49], v[48:49], v[152:153] op_sel_hi:[1,0]
	v_cvt_pk_bf16_f32 v54, v54, v55
	v_cvt_pk_bf16_f32 v55, v56, v57
	v_cvt_pk_bf16_f32 v56, v46, v47
	v_cvt_pk_bf16_f32 v57, v48, v49
	global_store_dwordx4 v[174:175], v[54:57], off offset:256
	s_mov_b64 s[40:41], 0xea000
	v_lshl_add_u64 v[176:177], v[172:173], 0, s[40:41]
	v_pk_mul_f32 v[50:51], v[50:51], v[154:155] op_sel_hi:[1,0]
	v_pk_mul_f32 v[52:53], v[52:53], v[154:155] op_sel_hi:[1,0]
	v_pk_mul_f32 v[42:43], v[42:43], v[154:155] op_sel_hi:[1,0]
	v_pk_mul_f32 v[44:45], v[44:45], v[154:155] op_sel_hi:[1,0]
	v_cvt_pk_bf16_f32 v50, v50, v51
	v_cvt_pk_bf16_f32 v51, v52, v53
	v_cvt_pk_bf16_f32 v52, v42, v43
	v_cvt_pk_bf16_f32 v53, v44, v45
	global_store_dwordx4 v[176:177], v[50:53], off
	v_pk_mul_f32 v[38:39], v[38:39], v[154:155] op_sel_hi:[1,0]
	v_pk_mul_f32 v[40:41], v[40:41], v[154:155] op_sel_hi:[1,0]
	v_pk_mul_f32 v[30:31], v[30:31], v[154:155] op_sel_hi:[1,0]
	v_pk_mul_f32 v[32:33], v[32:33], v[154:155] op_sel_hi:[1,0]
	v_cvt_pk_bf16_f32 v38, v38, v39
	v_cvt_pk_bf16_f32 v39, v40, v41
	v_cvt_pk_bf16_f32 v40, v30, v31
	v_cvt_pk_bf16_f32 v41, v32, v33
	global_store_dwordx4 v[176:177], v[38:41], off offset:256
	s_mov_b64 s[40:41], 0x104000
	v_lshl_add_u64 v[174:175], v[172:173], 0, s[40:41]
	v_pk_mul_f32 v[34:35], v[34:35], v[156:157] op_sel_hi:[1,0]
	v_pk_mul_f32 v[36:37], v[36:37], v[156:157] op_sel_hi:[1,0]
	v_pk_mul_f32 v[26:27], v[26:27], v[156:157] op_sel_hi:[1,0]
	v_pk_mul_f32 v[28:29], v[28:29], v[156:157] op_sel_hi:[1,0]
	v_cvt_pk_bf16_f32 v34, v34, v35
	v_cvt_pk_bf16_f32 v35, v36, v37
	v_cvt_pk_bf16_f32 v36, v26, v27
	v_cvt_pk_bf16_f32 v37, v28, v29
	global_store_dwordx4 v[174:175], v[34:37], off
	v_pk_mul_f32 v[22:23], v[22:23], v[156:157] op_sel_hi:[1,0]
	v_pk_mul_f32 v[24:25], v[24:25], v[156:157] op_sel_hi:[1,0]
	v_pk_mul_f32 v[14:15], v[14:15], v[156:157] op_sel_hi:[1,0]
	v_pk_mul_f32 v[16:17], v[16:17], v[156:157] op_sel_hi:[1,0]
	v_cvt_pk_bf16_f32 v22, v22, v23
	v_cvt_pk_bf16_f32 v23, v24, v25
	v_cvt_pk_bf16_f32 v24, v14, v15
	v_cvt_pk_bf16_f32 v25, v16, v17
	global_store_dwordx4 v[174:175], v[22:25], off offset:256
	s_mov_b64 s[40:41], 0x11e000
	v_lshl_add_u64 v[176:177], v[172:173], 0, s[40:41]
	v_pk_mul_f32 v[18:19], v[18:19], v[168:169] op_sel_hi:[1,0]
	v_pk_mul_f32 v[20:21], v[20:21], v[168:169] op_sel_hi:[1,0]
	v_pk_mul_f32 v[10:11], v[10:11], v[168:169] op_sel_hi:[1,0]
	v_pk_mul_f32 v[12:13], v[12:13], v[168:169] op_sel_hi:[1,0]
	v_cvt_pk_bf16_f32 v18, v18, v19
	v_cvt_pk_bf16_f32 v19, v20, v21
	v_cvt_pk_bf16_f32 v20, v10, v11
	v_cvt_pk_bf16_f32 v21, v12, v13
	global_store_dwordx4 v[176:177], v[18:21], off
	v_pk_mul_f32 v[6:7], v[6:7], v[168:169] op_sel_hi:[1,0]
	v_pk_mul_f32 v[8:9], v[8:9], v[168:169] op_sel_hi:[1,0]
	v_pk_mul_f32 v[2:3], v[2:3], v[168:169] op_sel_hi:[1,0]
	v_pk_mul_f32 v[4:5], v[4:5], v[168:169] op_sel_hi:[1,0]
	v_cvt_pk_bf16_f32 v6, v6, v7
	v_cvt_pk_bf16_f32 v7, v8, v9
	v_cvt_pk_bf16_f32 v8, v2, v3
	v_cvt_pk_bf16_f32 v9, v4, v5
	global_store_dwordx4 v[176:177], v[6:9], off offset:256
	s_nop 3
	v_mfma_f32_32x32x16_bf16 v[2:17], v[200:203], v[200:203], 0
	v_mfma_f32_32x32x16_bf16 v[18:33], v[200:203], v[200:203], 0
	v_mfma_f32_32x32x16_bf16 v[34:49], v[200:203], v[200:203], 0
	v_mfma_f32_32x32x16_bf16 v[50:65], v[200:203], v[200:203], 0
	v_mfma_f32_32x32x16_bf16 v[66:81], v[200:203], v[200:203], 0
	v_mfma_f32_32x32x16_bf16 v[82:97], v[200:203], v[200:203], 0
	v_mfma_f32_32x32x16_bf16 v[98:113], v[200:203], v[200:203], 0
	v_mfma_f32_32x32x16_bf16 v[114:129], v[200:203], v[200:203], 0
	s_andn2_b64 vcc, exec, s[38:39]
	s_mov_b64 s[6:7], -1
	s_cbranch_vccnz .LBB0_832
	s_andn2_b64 vcc, exec, s[12:13]
	s_cbranch_vccnz .LBB0_831
	s_barrier
	s_branch .LBB0_831

.LBB0_2625:
	s_ashr_i32 s21, s20, 31
	s_lshl_b64 s[22:23], s[20:21], 19
	s_add_u32 s22, s5, s22
	s_addc_u32 s23, s30, s23
	s_and_b64 s[24:25], s[38:39], exec
	s_cselect_b32 s21, s23, s27
	s_cselect_b32 s33, s22, s26
	s_ashr_i32 s19, s18, 31
	s_lshl_b64 s[24:25], s[18:19], 19
	s_add_u32 s24, s31, s24
	s_addc_u32 s25, s34, s25
	s_and_b64 s[28:29], s[38:39], exec
	s_cselect_b32 s19, s25, s7
	s_cselect_b32 s40, s24, s6
	s_add_u32 s41, s6, 0x100
	s_addc_u32 s48, s7, 0
	s_add_u32 s6, s26, 0x40080
	v_mov_b32_e32 v2, 0
	s_addc_u32 s7, s27, 0
	s_mov_b32 s49, -2
	s_cmp_lg_u32 s46, 1
	s_cbranch_scc1 .Lskipz_c6
	v_mov_b32_e32 v3, v2
	v_mov_b32_e32 v4, v2
	v_mov_b32_e32 v5, v2
	v_mov_b32_e32 v6, v2
	v_mov_b32_e32 v7, v2
	v_mov_b32_e32 v8, v2
	v_mov_b32_e32 v9, v2
	v_mov_b32_e32 v18, v2
	v_mov_b32_e32 v19, v2
	v_mov_b32_e32 v20, v2
	v_mov_b32_e32 v21, v2
	v_mov_b32_e32 v22, v2
	v_mov_b32_e32 v23, v2
	v_mov_b32_e32 v24, v2
	v_mov_b32_e32 v25, v2
	v_mov_b32_e32 v34, v2
	v_mov_b32_e32 v35, v2
	v_mov_b32_e32 v36, v2
	v_mov_b32_e32 v37, v2
	v_mov_b32_e32 v38, v2
	v_mov_b32_e32 v39, v2
	v_mov_b32_e32 v40, v2
	v_mov_b32_e32 v41, v2
	v_mov_b32_e32 v50, v2
	v_mov_b32_e32 v51, v2
	v_mov_b32_e32 v52, v2
	v_mov_b32_e32 v53, v2
	v_mov_b32_e32 v54, v2
	v_mov_b32_e32 v55, v2
	v_mov_b32_e32 v56, v2
	v_mov_b32_e32 v57, v2
	v_mov_b32_e32 v10, v2
	v_mov_b32_e32 v11, v2
	v_mov_b32_e32 v12, v2
	v_mov_b32_e32 v13, v2
	v_mov_b32_e32 v14, v2
	v_mov_b32_e32 v15, v2
	v_mov_b32_e32 v16, v2
	v_mov_b32_e32 v17, v2
	v_mov_b32_e32 v26, v2
	v_mov_b32_e32 v27, v2
	v_mov_b32_e32 v28, v2
	v_mov_b32_e32 v29, v2
	v_mov_b32_e32 v30, v2
	v_mov_b32_e32 v31, v2
	v_mov_b32_e32 v32, v2
	v_mov_b32_e32 v33, v2
	v_mov_b32_e32 v42, v2
	v_mov_b32_e32 v43, v2
	v_mov_b32_e32 v44, v2
	v_mov_b32_e32 v45, v2
	v_mov_b32_e32 v46, v2
	v_mov_b32_e32 v47, v2
	v_mov_b32_e32 v48, v2
	v_mov_b32_e32 v49, v2
	v_mov_b32_e32 v58, v2
	v_mov_b32_e32 v59, v2
	v_mov_b32_e32 v60, v2
	v_mov_b32_e32 v61, v2
	v_mov_b32_e32 v62, v2
	v_mov_b32_e32 v63, v2
	v_mov_b32_e32 v64, v2
	v_mov_b32_e32 v65, v2
	v_mov_b32_e32 v66, v2
	v_mov_b32_e32 v67, v2
	v_mov_b32_e32 v68, v2
	v_mov_b32_e32 v69, v2
	v_mov_b32_e32 v70, v2
	v_mov_b32_e32 v71, v2
	v_mov_b32_e32 v72, v2
	v_mov_b32_e32 v73, v2
	v_mov_b32_e32 v82, v2
	v_mov_b32_e32 v83, v2
	v_mov_b32_e32 v84, v2
	v_mov_b32_e32 v85, v2
	v_mov_b32_e32 v86, v2
	v_mov_b32_e32 v87, v2
	v_mov_b32_e32 v88, v2
	v_mov_b32_e32 v89, v2
	v_mov_b32_e32 v98, v2
	v_mov_b32_e32 v99, v2
	v_mov_b32_e32 v100, v2
	v_mov_b32_e32 v101, v2
	v_mov_b32_e32 v102, v2
	v_mov_b32_e32 v103, v2
	v_mov_b32_e32 v104, v2
	v_mov_b32_e32 v105, v2
	v_mov_b32_e32 v114, v2
	v_mov_b32_e32 v115, v2
	v_mov_b32_e32 v116, v2
	v_mov_b32_e32 v117, v2
	v_mov_b32_e32 v118, v2
	v_mov_b32_e32 v119, v2
	v_mov_b32_e32 v120, v2
	v_mov_b32_e32 v121, v2
	v_mov_b32_e32 v74, v2
	v_mov_b32_e32 v75, v2
	v_mov_b32_e32 v76, v2
	v_mov_b32_e32 v77, v2
	v_mov_b32_e32 v78, v2
	v_mov_b32_e32 v79, v2
	v_mov_b32_e32 v80, v2
	v_mov_b32_e32 v81, v2
	v_mov_b32_e32 v90, v2
	v_mov_b32_e32 v91, v2
	v_mov_b32_e32 v92, v2
	v_mov_b32_e32 v93, v2
	v_mov_b32_e32 v94, v2
	v_mov_b32_e32 v95, v2
	v_mov_b32_e32 v96, v2
	v_mov_b32_e32 v97, v2
	v_mov_b32_e32 v106, v2
	v_mov_b32_e32 v107, v2
	v_mov_b32_e32 v108, v2
	v_mov_b32_e32 v109, v2
	v_mov_b32_e32 v110, v2
	v_mov_b32_e32 v111, v2
	v_mov_b32_e32 v112, v2
	v_mov_b32_e32 v113, v2
	v_mov_b32_e32 v122, v2
	v_mov_b32_e32 v123, v2
	v_mov_b32_e32 v124, v2
	v_mov_b32_e32 v125, v2
	v_mov_b32_e32 v126, v2
	v_mov_b32_e32 v127, v2
	v_mov_b32_e32 v128, v2
	v_mov_b32_e32 v129, v2
.Lskipz_c6:
	v_and_b32_e32 v130, 8, v182
	v_and_b32_e32 v131, 16, v182
	v_lshlrev_b32_e32 v130, 2, v130
	v_lshl_add_u32 v130, v131, 3, v130
	v_lshl_add_u32 v131, s4, 8, v180
	v_add_u32_e32 v130, v130, v131
	v_mov_b32_e32 v131, 0
	v_lshl_add_u64 v[130:131], v[130:131], 4, s[14:15]
	global_load_dwordx4 v[240:243], v[130:131], off
	global_load_dwordx2 v[244:245], v[130:131], off offset:256
	global_load_dword v239, v[130:131], off offset:264

.LBB0_2629:
	v_mov_b32_e32 v204, 0
	v_mov_b32_e32 v205, 0
	v_mov_b32_e32 v206, 0
	v_mov_b32_e32 v207, 0
	v_lshl_add_u32 v178, s4, 8, v180
	v_and_b32_e32 v130, 8, v182
	v_and_b32_e32 v131, 16, v182
	v_lshlrev_b32_e32 v130, 2, v130
	v_lshl_add_u32 v130, v131, 3, v130
	v_add_u32_e32 v130, v130, v178
	v_mov_b32_e32 v131, 0
	v_lshl_add_u64 v[130:131], v[130:131], 4, s[14:15]
	global_load_dword v140, v[130:131], off offset:268
	s_waitcnt vmcnt(9)
	v_add_f32_e32 v240, v240, v241
	v_add_f32_e32 v242, v242, v243
	v_add_f32_e32 v240, v240, v242
	v_fmamk_f32 v240, v240, 0x3a800000, v226
	v_rsq_f32_e32 v240, v240
	v_and_b32_e32 v190, 15, v180
	v_lshlrev_b32_e32 v190, 2, v190
	v_add_u32_e32 v191, 64, v190
	v_add_u32_e32 v192, 0x80, v190
	v_add_u32_e32 v193, 0xc0, v190
	ds_bpermute_b32 v144, v190, v240
	ds_bpermute_b32 v148, v191, v240
	ds_bpermute_b32 v152, v192, v240
	ds_bpermute_b32 v156, v193, v240
	v_lshl_or_b32 v170, s47, 8, v182
	v_lshlrev_b32_e32 v170, 1, v170
	v_mov_b32_e32 v171, 0
	v_mov_b32_e32 v179, 0
	v_lshlrev_b64 v[172:173], 13, v[178:179]
	v_lshl_add_u64 v[172:173], s[12:13], 0, v[172:173]
	v_lshl_add_u64 v[172:173], v[172:173], 0, v[170:171]
	s_waitcnt lgkmcnt(0)
	v_pk_mul_f32 v[126:127], v[126:127], v[144:145] op_sel_hi:[1,0]
	v_pk_mul_f32 v[128:129], v[128:129], v[144:145] op_sel_hi:[1,0]
	v_pk_mul_f32 v[122:123], v[122:123], v[144:145] op_sel_hi:[1,0]
	v_pk_mul_f32 v[124:125], v[124:125], v[144:145] op_sel_hi:[1,0]
	v_max_f32_e32 v132, 0, v126
	v_max_f32_e32 v133, 0, v127
	v_max_f32_e32 v134, 0, v128
	v_max_f32_e32 v135, 0, v129
	v_max_f32_e32 v136, 0, v122
	v_max_f32_e32 v137, 0, v123
	v_max_f32_e32 v138, 0, v124
	v_max_f32_e32 v139, 0, v125
	v_pk_mul_f32 v[126:127], v[126:127], v[132:133]
	v_pk_mul_f32 v[128:129], v[128:129], v[134:135]
	v_pk_mul_f32 v[122:123], v[122:123], v[136:137]
	v_pk_mul_f32 v[124:125], v[124:125], v[138:139]
	v_cvt_pk_bf16_f32 v126, v126, v127
	v_cvt_pk_bf16_f32 v127, v128, v129
	v_cvt_pk_bf16_f32 v128, v122, v123
	v_cvt_pk_bf16_f32 v129, v124, v125
	global_store_dwordx4 v[172:173], v[126:129], off
	v_pk_mul_f32 v[118:119], v[118:119], v[144:145] op_sel_hi:[1,0]
	v_pk_mul_f32 v[120:121], v[120:121], v[144:145] op_sel_hi:[1,0]
	v_pk_mul_f32 v[114:115], v[114:115], v[144:145] op_sel_hi:[1,0]
	v_pk_mul_f32 v[116:117], v[116:117], v[144:145] op_sel_hi:[1,0]
	v_max_f32_e32 v132, 0, v118
	v_max_f32_e32 v133, 0, v119
	v_max_f32_e32 v134, 0, v120
	v_max_f32_e32 v135, 0, v121
	v_max_f32_e32 v136, 0, v114
	v_max_f32_e32 v137, 0, v115
	v_max_f32_e32 v138, 0, v116
	v_max_f32_e32 v139, 0, v117
	v_pk_mul_f32 v[118:119], v[118:119], v[132:133]
	v_pk_mul_f32 v[120:121], v[120:121], v[134:135]
	v_pk_mul_f32 v[114:115], v[114:115], v[136:137]
	v_pk_mul_f32 v[116:117], v[116:117], v[138:139]
	v_cvt_pk_bf16_f32 v118, v118, v119
	v_cvt_pk_bf16_f32 v119, v120, v121
	v_cvt_pk_bf16_f32 v120, v114, v115
	v_cvt_pk_bf16_f32 v121, v116, v117
	global_store_dwordx4 v[172:173], v[118:121], off offset:256
	s_mov_b64 s[40:41], 0x40000
	v_lshl_add_u64 v[176:177], v[172:173], 0, s[40:41]
	v_pk_mul_f32 v[94:95], v[94:95], v[148:149] op_sel_hi:[1,0]
	v_pk_mul_f32 v[96:97], v[96:97], v[148:149] op_sel_hi:[1,0]
	v_pk_mul_f32 v[90:91], v[90:91], v[148:149] op_sel_hi:[1,0]
	v_pk_mul_f32 v[92:93], v[92:93], v[148:149] op_sel_hi:[1,0]
	v_max_f32_e32 v132, 0, v94
	v_max_f32_e32 v133, 0, v95
	v_max_f32_e32 v134, 0, v96
	v_max_f32_e32 v135, 0, v97
	v_max_f32_e32 v136, 0, v90
	v_max_f32_e32 v137, 0, v91
	v_max_f32_e32 v138, 0, v92
	v_max_f32_e32 v139, 0, v93
	v_pk_mul_f32 v[94:95], v[94:95], v[132:133]
	v_pk_mul_f32 v[96:97], v[96:97], v[134:135]
	v_pk_mul_f32 v[90:91], v[90:91], v[136:137]
	v_pk_mul_f32 v[92:93], v[92:93], v[138:139]
	v_cvt_pk_bf16_f32 v94, v94, v95
	v_cvt_pk_bf16_f32 v95, v96, v97
	v_cvt_pk_bf16_f32 v96, v90, v91
	v_cvt_pk_bf16_f32 v97, v92, v93
	global_store_dwordx4 v[176:177], v[94:97], off
	v_pk_mul_f32 v[86:87], v[86:87], v[148:149] op_sel_hi:[1,0]
	v_pk_mul_f32 v[88:89], v[88:89], v[148:149] op_sel_hi:[1,0]
	v_pk_mul_f32 v[82:83], v[82:83], v[148:149] op_sel_hi:[1,0]
	v_pk_mul_f32 v[84:85], v[84:85], v[148:149] op_sel_hi:[1,0]
	v_max_f32_e32 v132, 0, v86
	v_max_f32_e32 v133, 0, v87
	v_max_f32_e32 v134, 0, v88
	v_max_f32_e32 v135, 0, v89
	v_max_f32_e32 v136, 0, v82
	v_max_f32_e32 v137, 0, v83
	v_max_f32_e32 v138, 0, v84
	v_max_f32_e32 v139, 0, v85
	v_pk_mul_f32 v[86:87], v[86:87], v[132:133]
	v_pk_mul_f32 v[88:89], v[88:89], v[134:135]
	v_pk_mul_f32 v[82:83], v[82:83], v[136:137]
	v_pk_mul_f32 v[84:85], v[84:85], v[138:139]
	v_cvt_pk_bf16_f32 v86, v86, v87
	v_cvt_pk_bf16_f32 v87, v88, v89
	v_cvt_pk_bf16_f32 v88, v82, v83
	v_cvt_pk_bf16_f32 v89, v84, v85
	global_store_dwordx4 v[176:177], v[86:89], off offset:256
	s_mov_b64 s[40:41], 0x100000
	v_lshl_add_u64 v[174:175], v[172:173], 0, s[40:41]
	v_pk_mul_f32 v[62:63], v[62:63], v[152:153] op_sel_hi:[1,0]
	v_pk_mul_f32 v[64:65], v[64:65], v[152:153] op_sel_hi:[1,0]
	v_pk_mul_f32 v[58:59], v[58:59], v[152:153] op_sel_hi:[1,0]
	v_pk_mul_f32 v[60:61], v[60:61], v[152:153] op_sel_hi:[1,0]
	v_max_f32_e32 v132, 0, v62
	v_max_f32_e32 v133, 0, v63
	v_max_f32_e32 v134, 0, v64
	v_max_f32_e32 v135, 0, v65
	v_max_f32_e32 v136, 0, v58
	v_max_f32_e32 v137, 0, v59
	v_max_f32_e32 v138, 0, v60
	v_max_f32_e32 v139, 0, v61
	v_pk_mul_f32 v[62:63], v[62:63], v[132:133]
	v_pk_mul_f32 v[64:65], v[64:65], v[134:135]
	v_pk_mul_f32 v[58:59], v[58:59], v[136:137]
	v_pk_mul_f32 v[60:61], v[60:61], v[138:139]
	v_cvt_pk_bf16_f32 v62, v62, v63
	v_cvt_pk_bf16_f32 v63, v64, v65
	v_cvt_pk_bf16_f32 v64, v58, v59
	v_cvt_pk_bf16_f32 v65, v60, v61
	global_store_dwordx4 v[174:175], v[62:65], off
	v_pk_mul_f32 v[54:55], v[54:55], v[152:153] op_sel_hi:[1,0]
	v_pk_mul_f32 v[56:57], v[56:57], v[152:153] op_sel_hi:[1,0]
	v_pk_mul_f32 v[50:51], v[50:51], v[152:153] op_sel_hi:[1,0]
	v_pk_mul_f32 v[52:53], v[52:53], v[152:153] op_sel_hi:[1,0]
	v_max_f32_e32 v132, 0, v54
	v_max_f32_e32 v133, 0, v55
	v_max_f32_e32 v134, 0, v56
	v_max_f32_e32 v135, 0, v57
	v_max_f32_e32 v136, 0, v50
	v_max_f32_e32 v137, 0, v51
	v_max_f32_e32 v138, 0, v52
	v_max_f32_e32 v139, 0, v53
	v_pk_mul_f32 v[54:55], v[54:55], v[132:133]
	v_pk_mul_f32 v[56:57], v[56:57], v[134:135]
	v_pk_mul_f32 v[50:51], v[50:51], v[136:137]
	v_pk_mul_f32 v[52:53], v[52:53], v[138:139]
	v_cvt_pk_bf16_f32 v54, v54, v55
	v_cvt_pk_bf16_f32 v55, v56, v57
	v_cvt_pk_bf16_f32 v56, v50, v51
	v_cvt_pk_bf16_f32 v57, v52, v53
	global_store_dwordx4 v[174:175], v[54:57], off offset:256
	s_mov_b64 s[40:41], 0x140000
	v_lshl_add_u64 v[176:177], v[172:173], 0, s[40:41]
	v_pk_mul_f32 v[30:31], v[30:31], v[156:157] op_sel_hi:[1,0]
	v_pk_mul_f32 v[32:33], v[32:33], v[156:157] op_sel_hi:[1,0]
	v_pk_mul_f32 v[26:27], v[26:27], v[156:157] op_sel_hi:[1,0]
	v_pk_mul_f32 v[28:29], v[28:29], v[156:157] op_sel_hi:[1,0]
	v_max_f32_e32 v132, 0, v30
	v_max_f32_e32 v133, 0, v31
	v_max_f32_e32 v134, 0, v32
	v_max_f32_e32 v135, 0, v33
	v_max_f32_e32 v136, 0, v26
	v_max_f32_e32 v137, 0, v27
	v_max_f32_e32 v138, 0, v28
	v_max_f32_e32 v139, 0, v29
	v_pk_mul_f32 v[30:31], v[30:31], v[132:133]
	v_pk_mul_f32 v[32:33], v[32:33], v[134:135]
	v_pk_mul_f32 v[26:27], v[26:27], v[136:137]
	v_pk_mul_f32 v[28:29], v[28:29], v[138:139]
	v_cvt_pk_bf16_f32 v30, v30, v31
	v_cvt_pk_bf16_f32 v31, v32, v33
	v_cvt_pk_bf16_f32 v32, v26, v27
	v_cvt_pk_bf16_f32 v33, v28, v29
	global_store_dwordx4 v[176:177], v[30:33], off
	v_pk_mul_f32 v[22:23], v[22:23], v[156:157] op_sel_hi:[1,0]
	v_pk_mul_f32 v[24:25], v[24:25], v[156:157] op_sel_hi:[1,0]
	v_pk_mul_f32 v[18:19], v[18:19], v[156:157] op_sel_hi:[1,0]
	v_pk_mul_f32 v[20:21], v[20:21], v[156:157] op_sel_hi:[1,0]
	v_max_f32_e32 v132, 0, v22
	v_max_f32_e32 v133, 0, v23
	v_max_f32_e32 v134, 0, v24
	v_max_f32_e32 v135, 0, v25
	v_max_f32_e32 v136, 0, v18
	v_max_f32_e32 v137, 0, v19
	v_max_f32_e32 v138, 0, v20
	v_max_f32_e32 v139, 0, v21
	v_pk_mul_f32 v[22:23], v[22:23], v[132:133]
	v_pk_mul_f32 v[24:25], v[24:25], v[134:135]
	v_pk_mul_f32 v[18:19], v[18:19], v[136:137]
	v_pk_mul_f32 v[20:21], v[20:21], v[138:139]
	v_cvt_pk_bf16_f32 v22, v22, v23
	v_cvt_pk_bf16_f32 v23, v24, v25
	v_cvt_pk_bf16_f32 v24, v18, v19
	v_cvt_pk_bf16_f32 v25, v20, v21
	global_store_dwordx4 v[176:177], v[22:25], off offset:256
	s_waitcnt vmcnt(8)
	v_add_f32_e32 v244, v244, v245
	v_add_f32_e32 v239, v239, v140
	v_add_f32_e32 v244, v244, v239
	v_fmamk_f32 v244, v244, 0x3a800000, v226
	v_rsq_f32_e32 v244, v244
	s_nop 0
	ds_bpermute_b32 v146, v190, v244
	ds_bpermute_b32 v150, v191, v244
	ds_bpermute_b32 v154, v192, v244
	ds_bpermute_b32 v194, v193, v244
	s_waitcnt lgkmcnt(0)
	s_mov_b64 s[40:41], 0x20000
	v_lshl_add_u64 v[174:175], v[172:173], 0, s[40:41]
	v_pk_mul_f32 v[110:111], v[110:111], v[146:147] op_sel_hi:[1,0]
	v_pk_mul_f32 v[112:113], v[112:113], v[146:147] op_sel_hi:[1,0]
	v_pk_mul_f32 v[106:107], v[106:107], v[146:147] op_sel_hi:[1,0]
	v_pk_mul_f32 v[108:109], v[108:109], v[146:147] op_sel_hi:[1,0]
	v_max_f32_e32 v132, 0, v110
	v_max_f32_e32 v133, 0, v111
	v_max_f32_e32 v134, 0, v112
	v_max_f32_e32 v135, 0, v113
	v_max_f32_e32 v136, 0, v106
	v_max_f32_e32 v137, 0, v107
	v_max_f32_e32 v138, 0, v108
	v_max_f32_e32 v139, 0, v109
	v_pk_mul_f32 v[110:111], v[110:111], v[132:133]
	v_pk_mul_f32 v[112:113], v[112:113], v[134:135]
	v_pk_mul_f32 v[106:107], v[106:107], v[136:137]
	v_pk_mul_f32 v[108:109], v[108:109], v[138:139]
	v_cvt_pk_bf16_f32 v110, v110, v111
	v_cvt_pk_bf16_f32 v111, v112, v113
	v_cvt_pk_bf16_f32 v112, v106, v107
	v_cvt_pk_bf16_f32 v113, v108, v109
	global_store_dwordx4 v[174:175], v[110:113], off
	v_pk_mul_f32 v[102:103], v[102:103], v[146:147] op_sel_hi:[1,0]
	v_pk_mul_f32 v[104:105], v[104:105], v[146:147] op_sel_hi:[1,0]
	v_pk_mul_f32 v[98:99], v[98:99], v[146:147] op_sel_hi:[1,0]
	v_pk_mul_f32 v[100:101], v[100:101], v[146:147] op_sel_hi:[1,0]
	v_max_f32_e32 v132, 0, v102
	v_max_f32_e32 v133, 0, v103
	v_max_f32_e32 v134, 0, v104
	v_max_f32_e32 v135, 0, v105
	v_max_f32_e32 v136, 0, v98
	v_max_f32_e32 v137, 0, v99
	v_max_f32_e32 v138, 0, v100
	v_max_f32_e32 v139, 0, v101
	v_pk_mul_f32 v[102:103], v[102:103], v[132:133]
	v_pk_mul_f32 v[104:105], v[104:105], v[134:135]
	v_pk_mul_f32 v[98:99], v[98:99], v[136:137]
	v_pk_mul_f32 v[100:101], v[100:101], v[138:139]
	v_cvt_pk_bf16_f32 v102, v102, v103
	v_cvt_pk_bf16_f32 v103, v104, v105
	v_cvt_pk_bf16_f32 v104, v98, v99
	v_cvt_pk_bf16_f32 v105, v100, v101
	global_store_dwordx4 v[174:175], v[102:105], off offset:256
	s_mov_b64 s[40:41], 0x60000
	v_lshl_add_u64 v[176:177], v[172:173], 0, s[40:41]
	v_pk_mul_f32 v[78:79], v[78:79], v[150:151] op_sel_hi:[1,0]
	v_pk_mul_f32 v[80:81], v[80:81], v[150:151] op_sel_hi:[1,0]
	v_pk_mul_f32 v[74:75], v[74:75], v[150:151] op_sel_hi:[1,0]
	v_pk_mul_f32 v[76:77], v[76:77], v[150:151] op_sel_hi:[1,0]
	v_max_f32_e32 v132, 0, v78
	v_max_f32_e32 v133, 0, v79
	v_max_f32_e32 v134, 0, v80
	v_max_f32_e32 v135, 0, v81
	v_max_f32_e32 v136, 0, v74
	v_max_f32_e32 v137, 0, v75
	v_max_f32_e32 v138, 0, v76
	v_max_f32_e32 v139, 0, v77
	v_pk_mul_f32 v[78:79], v[78:79], v[132:133]
	v_pk_mul_f32 v[80:81], v[80:81], v[134:135]
	v_pk_mul_f32 v[74:75], v[74:75], v[136:137]
	v_pk_mul_f32 v[76:77], v[76:77], v[138:139]
	v_cvt_pk_bf16_f32 v78, v78, v79
	v_cvt_pk_bf16_f32 v79, v80, v81
	v_cvt_pk_bf16_f32 v80, v74, v75
	v_cvt_pk_bf16_f32 v81, v76, v77
	global_store_dwordx4 v[176:177], v[78:81], off
	v_pk_mul_f32 v[70:71], v[70:71], v[150:151] op_sel_hi:[1,0]
	v_pk_mul_f32 v[72:73], v[72:73], v[150:151] op_sel_hi:[1,0]
	v_pk_mul_f32 v[66:67], v[66:67], v[150:151] op_sel_hi:[1,0]
	v_pk_mul_f32 v[68:69], v[68:69], v[150:151] op_sel_hi:[1,0]
	v_max_f32_e32 v132, 0, v70
	v_max_f32_e32 v133, 0, v71
	v_max_f32_e32 v134, 0, v72
	v_max_f32_e32 v135, 0, v73
	v_max_f32_e32 v136, 0, v66
	v_max_f32_e32 v137, 0, v67
	v_max_f32_e32 v138, 0, v68
	v_max_f32_e32 v139, 0, v69
	v_pk_mul_f32 v[70:71], v[70:71], v[132:133]
	v_pk_mul_f32 v[72:73], v[72:73], v[134:135]
	v_pk_mul_f32 v[66:67], v[66:67], v[136:137]
	v_pk_mul_f32 v[68:69], v[68:69], v[138:139]
	v_cvt_pk_bf16_f32 v70, v70, v71
	v_cvt_pk_bf16_f32 v71, v72, v73
	v_cvt_pk_bf16_f32 v72, v66, v67
	v_cvt_pk_bf16_f32 v73, v68, v69
	global_store_dwordx4 v[176:177], v[70:73], off offset:256
	s_mov_b64 s[40:41], 0x120000
	v_lshl_add_u64 v[174:175], v[172:173], 0, s[40:41]
	v_pk_mul_f32 v[46:47], v[46:47], v[154:155] op_sel_hi:[1,0]
	v_pk_mul_f32 v[48:49], v[48:49], v[154:155] op_sel_hi:[1,0]
	v_pk_mul_f32 v[42:43], v[42:43], v[154:155] op_sel_hi:[1,0]
	v_pk_mul_f32 v[44:45], v[44:45], v[154:155] op_sel_hi:[1,0]
	v_max_f32_e32 v132, 0, v46
	v_max_f32_e32 v133, 0, v47
	v_max_f32_e32 v134, 0, v48
	v_max_f32_e32 v135, 0, v49
	v_max_f32_e32 v136, 0, v42
	v_max_f32_e32 v137, 0, v43
	v_max_f32_e32 v138, 0, v44
	v_max_f32_e32 v139, 0, v45
	v_pk_mul_f32 v[46:47], v[46:47], v[132:133]
	v_pk_mul_f32 v[48:49], v[48:49], v[134:135]
	v_pk_mul_f32 v[42:43], v[42:43], v[136:137]
	v_pk_mul_f32 v[44:45], v[44:45], v[138:139]
	v_cvt_pk_bf16_f32 v46, v46, v47
	v_cvt_pk_bf16_f32 v47, v48, v49
	v_cvt_pk_bf16_f32 v48, v42, v43
	v_cvt_pk_bf16_f32 v49, v44, v45
	global_store_dwordx4 v[174:175], v[46:49], off
	v_pk_mul_f32 v[38:39], v[38:39], v[154:155] op_sel_hi:[1,0]
	v_pk_mul_f32 v[40:41], v[40:41], v[154:155] op_sel_hi:[1,0]
	v_pk_mul_f32 v[34:35], v[34:35], v[154:155] op_sel_hi:[1,0]
	v_pk_mul_f32 v[36:37], v[36:37], v[154:155] op_sel_hi:[1,0]
	v_max_f32_e32 v132, 0, v38
	v_max_f32_e32 v133, 0, v39
	v_max_f32_e32 v134, 0, v40
	v_max_f32_e32 v135, 0, v41
	v_max_f32_e32 v136, 0, v34
	v_max_f32_e32 v137, 0, v35
	v_max_f32_e32 v138, 0, v36
	v_max_f32_e32 v139, 0, v37
	v_pk_mul_f32 v[38:39], v[38:39], v[132:133]
	v_pk_mul_f32 v[40:41], v[40:41], v[134:135]
	v_pk_mul_f32 v[34:35], v[34:35], v[136:137]
	v_pk_mul_f32 v[36:37], v[36:37], v[138:139]
	v_cvt_pk_bf16_f32 v38, v38, v39
	v_cvt_pk_bf16_f32 v39, v40, v41
	v_cvt_pk_bf16_f32 v40, v34, v35
	v_cvt_pk_bf16_f32 v41, v36, v37
	global_store_dwordx4 v[174:175], v[38:41], off offset:256
	s_mov_b64 s[40:41], 0x160000
	v_lshl_add_u64 v[176:177], v[172:173], 0, s[40:41]
	v_pk_mul_f32 v[14:15], v[14:15], v[194:195] op_sel_hi:[1,0]
	v_pk_mul_f32 v[16:17], v[16:17], v[194:195] op_sel_hi:[1,0]
	v_pk_mul_f32 v[10:11], v[10:11], v[194:195] op_sel_hi:[1,0]
	v_pk_mul_f32 v[12:13], v[12:13], v[194:195] op_sel_hi:[1,0]
	v_max_f32_e32 v132, 0, v14
	v_max_f32_e32 v133, 0, v15
	v_max_f32_e32 v134, 0, v16
	v_max_f32_e32 v135, 0, v17
	v_max_f32_e32 v136, 0, v10
	v_max_f32_e32 v137, 0, v11
	v_max_f32_e32 v138, 0, v12
	v_max_f32_e32 v139, 0, v13
	v_pk_mul_f32 v[14:15], v[14:15], v[132:133]
	v_pk_mul_f32 v[16:17], v[16:17], v[134:135]
	v_pk_mul_f32 v[10:11], v[10:11], v[136:137]
	v_pk_mul_f32 v[12:13], v[12:13], v[138:139]
	v_cvt_pk_bf16_f32 v14, v14, v15
	v_cvt_pk_bf16_f32 v15, v16, v17
	v_cvt_pk_bf16_f32 v16, v10, v11
	v_cvt_pk_bf16_f32 v17, v12, v13
	global_store_dwordx4 v[176:177], v[14:17], off
	v_pk_mul_f32 v[6:7], v[6:7], v[194:195] op_sel_hi:[1,0]
	v_pk_mul_f32 v[8:9], v[8:9], v[194:195] op_sel_hi:[1,0]
	v_pk_mul_f32 v[2:3], v[2:3], v[194:195] op_sel_hi:[1,0]
	v_pk_mul_f32 v[4:5], v[4:5], v[194:195] op_sel_hi:[1,0]
	v_max_f32_e32 v132, 0, v6
	v_max_f32_e32 v133, 0, v7
	v_max_f32_e32 v134, 0, v8
	v_max_f32_e32 v135, 0, v9
	v_max_f32_e32 v136, 0, v2
	v_max_f32_e32 v137, 0, v3
	v_max_f32_e32 v138, 0, v4
	v_max_f32_e32 v139, 0, v5
	v_pk_mul_f32 v[6:7], v[6:7], v[132:133]
	v_pk_mul_f32 v[8:9], v[8:9], v[134:135]
	v_pk_mul_f32 v[2:3], v[2:3], v[136:137]
	v_pk_mul_f32 v[4:5], v[4:5], v[138:139]
	v_cvt_pk_bf16_f32 v6, v6, v7
	v_cvt_pk_bf16_f32 v7, v8, v9
	v_cvt_pk_bf16_f32 v8, v2, v3
	v_cvt_pk_bf16_f32 v9, v4, v5
	global_store_dwordx4 v[176:177], v[6:9], off offset:256
	s_nop 3
	v_mfma_f32_32x32x16_bf16 v[2:17], v[204:207], v[204:207], 0
	v_mfma_f32_32x32x16_bf16 v[18:33], v[204:207], v[204:207], 0
	v_mfma_f32_32x32x16_bf16 v[34:49], v[204:207], v[204:207], 0
	v_mfma_f32_32x32x16_bf16 v[50:65], v[204:207], v[204:207], 0
	v_mfma_f32_32x32x16_bf16 v[66:81], v[204:207], v[204:207], 0
	v_mfma_f32_32x32x16_bf16 v[82:97], v[204:207], v[204:207], 0
	v_mfma_f32_32x32x16_bf16 v[98:113], v[204:207], v[204:207], 0
	v_mfma_f32_32x32x16_bf16 v[114:129], v[204:207], v[204:207], 0
	s_mov_b64 s[6:7], -1
	s_andn2_b64 vcc, exec, s[38:39]
	s_cbranch_vccnz .LBB0_2618
	s_andn2_b64 vcc, exec, s[10:11]
	s_cbranch_vccnz .LBB0_2617
	s_barrier
	s_branch .LBB0_2617
